# ATT0 tile loop: in-wave MFMA/VALU interleave plus the mid-step K/V LDS-DMA issue sunk into the QK MFMA shadow (cold path keeps the original order for the last tile pair)
# speedup vs baseline: 1.0106x; 1.0106x over previous
.Latt0_nrA:
.LBB0_511:
	s_add_i32 s6, s19, -1
	s_min_u32 s36, s6, s42
	s_mul_i32 s6, s36, 0x30000
	s_add_u32 s6, s64, s6
	s_addc_u32 s7, s65, 0
	s_add_i32 s43, s19, -2
	s_waitcnt vmcnt(0)
	v_lshl_add_u64 v[204:205], s[6:7], 0, v[152:153]
	s_cmp_lt_u32 s43, s33
	s_waitcnt lgkmcnt(0)
	s_waitcnt vmcnt(0) lgkmcnt(0)
	s_barrier
	s_mov_b64 s[46:47], s[6:7]
	s_cselect_b64 s[6:7], -1, 0
	s_min_u32 s38, s43, s42
	s_lshl_b32 s38, s38, 19
	s_add_u32 s38, s66, s38
	s_addc_u32 s39, s67, 0
	s_cmp_ge_u32 s43, s33
	s_cbranch_scc1 .Latt0_cold_mid
	ds_read_b128 v[68:71], v185 offset:32768
	ds_read_b128 v[64:67], v184 offset:32768
	ds_read_b128 v[80:83], v184 offset:40960
	ds_read_b128 v[84:87], v186 offset:32768
	ds_read_b128 v[226:229], v188 offset:32768
	ds_read_b128 v[222:225], v187 offset:32768
	v_add_f32_e32 v204, 0, v112
	v_add_f32_e32 v204, v113, v204
	v_add_f32_e32 v204, v114, v204
	v_add_f32_e32 v204, v115, v204
	v_add_f32_e32 v204, v116, v204
	v_add_f32_e32 v204, v117, v204
	v_add_f32_e32 v204, v118, v204
	v_add_f32_e32 v204, v119, v204
	v_add_f32_e32 v204, v120, v204
	v_add_f32_e32 v204, v121, v204
	s_waitcnt lgkmcnt(0)
	v_mfma_f32_32x32x64_f8f6f4 v[64:79], v[64:71], v[128:135], 0
	v_lshl_add_u64 v[246:247], s[46:47], 0, v[152:153]
	s_mov_b32 m0, s95
	s_nop 0
	global_load_lds_dwordx4 v[246:247], off
	v_add_f32_e32 v204, v122, v204
	v_add_f32_e32 v204, v123, v204
	v_exp_f32_e32 v96, v96
	v_add_f32_e32 v204, v124, v204
	v_exp_f32_e32 v97, v97
	v_add_f32_e32 v204, v125, v204
	v_exp_f32_e32 v98, v98
	v_add_f32_e32 v204, v126, v204
	v_mfma_f32_32x32x64_f8f6f4 v[80:95], v[80:87], v[128:135], 0
	v_lshl_add_u64 v[246:247], s[46:47], 0, v[154:155]
	s_mov_b32 m0, s18
	s_nop 0
	global_load_lds_dwordx4 v[246:247], off
	v_exp_f32_e32 v99, v99
	v_add_f32_e32 v204, v127, v204
	v_exp_f32_e32 v100, v100
	v_add_f32_e32 v204, v96, v204
	v_exp_f32_e32 v101, v101
	v_add_f32_e32 v204, v97, v204
	v_exp_f32_e32 v102, v102
	v_add_f32_e32 v204, v98, v204
	v_mfma_f32_32x32x64_f8f6f4 v[64:79], v[222:229], v[136:143], v[64:79]
	v_lshl_add_u64 v[246:247], s[38:39], 0, v[156:157]
	s_mov_b32 m0, s56
	s_nop 0
	global_load_lds_dwordx4 v[246:247], off
	v_exp_f32_e32 v103, v103
	v_add_f32_e32 v204, v99, v204
	v_exp_f32_e32 v104, v104
	v_add_f32_e32 v204, v100, v204
	v_exp_f32_e32 v105, v105
	v_add_f32_e32 v204, v101, v204
	v_exp_f32_e32 v106, v106
	v_add_f32_e32 v204, v102, v204
	ds_read_b128 v[222:225], v187 offset:40960
	ds_read_b128 v[226:229], v189 offset:32768
	v_exp_f32_e32 v107, v107
	v_add_f32_e32 v204, v103, v204
	v_exp_f32_e32 v108, v108
	v_add_f32_e32 v204, v104, v204
	v_exp_f32_e32 v109, v109
	v_add_f32_e32 v204, v105, v204
	s_waitcnt lgkmcnt(0)
	v_mfma_f32_32x32x64_f8f6f4 v[80:95], v[222:229], v[136:143], v[80:95]
	v_lshl_add_u64 v[246:247], s[38:39], 0, v[158:159]
	s_mov_b32 m0, s91
	s_nop 0
	global_load_lds_dwordx4 v[246:247], off
	v_exp_f32_e32 v110, v110
	v_add_f32_e32 v204, v106, v204
	v_exp_f32_e32 v111, v111
	v_add_f32_e32 v204, v107, v204
	v_add_f32_e32 v204, v108, v204
	v_add_f32_e32 v204, v109, v204
	v_add_f32_e32 v204, v110, v204
	v_add_f32_e32 v204, v111, v204
	v_mov_b32_e32 v205, v204
	ds_read_b128 v[226:229], v192 offset:32768
	ds_read_b128 v[222:225], v191 offset:32768
	s_nop 1
	v_permlane32_swap_b32_e32 v204, v205
	v_cvt_pk_bf16_f32 v206, v112, v113
	v_cvt_pk_bf16_f32 v207, v114, v115
	v_cvt_pk_bf16_f32 v208, v116, v117
	v_cvt_pk_bf16_f32 v209, v118, v119
	v_cvt_pk_bf16_f32 v210, v120, v121
	v_cvt_pk_bf16_f32 v211, v122, v123
	s_waitcnt lgkmcnt(0)
	v_mfma_f32_32x32x64_f8f6f4 v[64:79], v[222:229], v[144:151], v[64:79]
	v_cvt_pk_bf16_f32 v212, v124, v125
	v_cvt_pk_bf16_f32 v213, v126, v127
	v_cvt_pk_bf16_f32 v214, v96, v97
	v_cvt_pk_bf16_f32 v215, v98, v99
	v_cvt_pk_bf16_f32 v216, v100, v101
	v_cvt_pk_bf16_f32 v217, v102, v103
	v_cvt_pk_bf16_f32 v218, v104, v105
	v_cvt_pk_bf16_f32 v219, v106, v107
	v_cvt_pk_bf16_f32 v220, v108, v109
	v_cvt_pk_bf16_f32 v221, v110, v111
	s_nop 0
	ds_read_b128 v[222:225], v191 offset:40960
	ds_read_b128 v[226:229], v193 offset:32768
	v_permlane32_swap_b32_e32 v206, v208
	v_permlane32_swap_b32_e32 v207, v209
	v_permlane32_swap_b32_e32 v210, v212
	v_permlane32_swap_b32_e32 v211, v213
	v_permlane32_swap_b32_e32 v214, v216
	s_waitcnt lgkmcnt(0)
	v_mfma_f32_32x32x64_f8f6f4 v[80:95], v[222:229], v[144:151], v[80:95]
	v_permlane32_swap_b32_e32 v215, v217
	v_permlane32_swap_b32_e32 v218, v220
	v_permlane32_swap_b32_e32 v219, v221
	ds_read_b64_tr_b16 v[222:223], v199 offset:0
	ds_read_b64_tr_b16 v[224:225], v199 offset:0x800
	ds_read_b64_tr_b16 v[226:227], v199 offset:0x1000
	ds_read_b64_tr_b16 v[228:229], v199 offset:0x1800
	ds_read_b64_tr_b16 v[230:231], v199 offset:0x2000
	ds_read_b64_tr_b16 v[232:233], v199 offset:0x2800
	ds_read_b64_tr_b16 v[234:235], v199 offset:0x3000
	ds_read_b64_tr_b16 v[236:237], v199 offset:0x3800
	v_max_f32_e32 v242, v65, v65
	v_max_f32_e32 v243, v64, v64
	v_max_f32_e32 v242, v243, v242
	v_max3_f32 v242, v242, v66, v67
	v_max3_f32 v242, v242, v68, v69
	v_max3_f32 v242, v242, v70, v71
	v_max3_f32 v242, v242, v72, v73
	v_max3_f32 v242, v242, v74, v75
	s_waitcnt lgkmcnt(0)
	s_nop 0
	v_mfma_f32_32x32x16_bf16 v[0:15], v[206:209], v[222:225], v[0:15]
	v_max3_f32 v242, v242, v76, v77
	v_max3_f32 v242, v242, v78, v79
	v_max3_f32 v242, v242, v80, v81
	v_max3_f32 v242, v242, v82, v83
	v_max3_f32 v242, v242, v84, v85
	ds_read_b64_tr_b16 v[222:223], v199 offset:0x200
	ds_read_b64_tr_b16 v[224:225], v199 offset:0xa00
	v_mfma_f32_32x32x16_bf16 v[0:15], v[210:213], v[226:229], v[0:15]
	v_max3_f32 v242, v242, v86, v87
	v_max3_f32 v242, v242, v88, v89
	v_max3_f32 v242, v242, v90, v91
	v_max3_f32 v242, v242, v92, v93
	v_max3_f32 v242, v242, v94, v95
	ds_read_b64_tr_b16 v[226:227], v199 offset:0x1200
	ds_read_b64_tr_b16 v[228:229], v199 offset:0x1a00
	v_mfma_f32_32x32x16_bf16 v[0:15], v[214:217], v[230:233], v[0:15]
	v_mov_b32_e32 v243, v242
	s_nop 1
	v_permlane32_swap_b32_e32 v242, v243
	ds_read_b64_tr_b16 v[230:231], v199 offset:0x2200
	ds_read_b64_tr_b16 v[232:233], v199 offset:0x2a00
	v_mfma_f32_32x32x16_bf16 v[0:15], v[218:221], v[234:237], v[0:15]
	v_max_f32_e32 v243, v243, v243
	v_max_f32_e32 v242, v242, v242
	v_max_f32_e32 v242, v242, v243
	v_sub_f32_e32 v243, v242, v195
	v_cmp_ge_f32_e32 vcc, s93, v243
	ds_read_b64_tr_b16 v[234:235], v199 offset:0x3200
	ds_read_b64_tr_b16 v[236:237], v199 offset:0x3a00
	v_max_f32_e32 v243, v195, v195
	v_max_f32_e32 v243, v243, v242
	v_sub_f32_e32 v242, v195, v243
	v_mul_f32_e32 v242, 0x3dd53b94, v242
	v_exp_f32_e32 v242, v242
	s_cmp_eq_u64 vcc, exec
	s_cselect_b64 s[6:7], -1, 0
	s_waitcnt lgkmcnt(0)
	v_mfma_f32_32x32x16_bf16 v[48:63], v[206:209], v[222:225], v[48:63]
	v_cndmask_b32_e64 v242, v242, 1.0, s[6:7]
	v_cmp_gt_f32_e32 vcc, 1.0, v242
	v_cndmask_b32_e64 v195, v243, v195, s[6:7]
	v_mul_f32_e32 v244, 0xbdd53b94, v195
	v_mov_b32_e32 v243, v244
	ds_read_b64_tr_b16 v[222:223], v199 offset:0x400
	ds_read_b64_tr_b16 v[224:225], v199 offset:0xc00
	v_mfma_f32_32x32x16_bf16 v[48:63], v[210:213], v[226:229], v[48:63]
	v_fmamk_f32 v64, v64, 0x3dd53b94, v244
	v_fmamk_f32 v65, v65, 0x3dd53b94, v244
	v_fmamk_f32 v66, v66, 0x3dd53b94, v244
	v_fmamk_f32 v67, v67, 0x3dd53b94, v244
	v_fmamk_f32 v68, v68, 0x3dd53b94, v244
	ds_read_b64_tr_b16 v[226:227], v199 offset:0x1400
	ds_read_b64_tr_b16 v[228:229], v199 offset:0x1c00
	v_mfma_f32_32x32x16_bf16 v[48:63], v[214:217], v[230:233], v[48:63]
	v_fmamk_f32 v69, v69, 0x3dd53b94, v244
	v_fmamk_f32 v70, v70, 0x3dd53b94, v244
	v_fmamk_f32 v71, v71, 0x3dd53b94, v244
	v_fmamk_f32 v72, v72, 0x3dd53b94, v244
	v_fmamk_f32 v73, v73, 0x3dd53b94, v244
	ds_read_b64_tr_b16 v[230:231], v199 offset:0x2400
	ds_read_b64_tr_b16 v[232:233], v199 offset:0x2c00
	v_mfma_f32_32x32x16_bf16 v[48:63], v[218:221], v[234:237], v[48:63]
	v_fmamk_f32 v74, v74, 0x3dd53b94, v244
	v_fmamk_f32 v75, v75, 0x3dd53b94, v244
	v_fmamk_f32 v76, v76, 0x3dd53b94, v244
	v_fmamk_f32 v77, v77, 0x3dd53b94, v244
	v_fmamk_f32 v78, v78, 0x3dd53b94, v244
	ds_read_b64_tr_b16 v[234:235], v199 offset:0x3400
	ds_read_b64_tr_b16 v[236:237], v199 offset:0x3c00
	v_fmac_f32_e32 v243, 0x3dd53b94, v79
	v_exp_f32_e32 v64, v64
	v_exp_f32_e32 v65, v65
	v_exp_f32_e32 v66, v66
	s_waitcnt lgkmcnt(0)
	v_mfma_f32_32x32x16_bf16 v[32:47], v[206:209], v[222:225], v[32:47]
	v_exp_f32_e32 v67, v67
	v_exp_f32_e32 v68, v68
	ds_read_b64_tr_b16 v[222:223], v199 offset:0x600
	ds_read_b64_tr_b16 v[224:225], v199 offset:0xe00
	v_mfma_f32_32x32x16_bf16 v[32:47], v[210:213], v[226:229], v[32:47]
	v_exp_f32_e32 v69, v69
	v_exp_f32_e32 v70, v70
	ds_read_b64_tr_b16 v[226:227], v199 offset:0x1600
	ds_read_b64_tr_b16 v[228:229], v199 offset:0x1e00
	v_mfma_f32_32x32x16_bf16 v[32:47], v[214:217], v[230:233], v[32:47]
	v_exp_f32_e32 v71, v71
	v_exp_f32_e32 v72, v72
	ds_read_b64_tr_b16 v[230:231], v199 offset:0x2600
	ds_read_b64_tr_b16 v[232:233], v199 offset:0x2e00
	v_mfma_f32_32x32x16_bf16 v[32:47], v[218:221], v[234:237], v[32:47]
	v_exp_f32_e32 v73, v73
	v_exp_f32_e32 v74, v74
	ds_read_b64_tr_b16 v[234:235], v199 offset:0x3600
	ds_read_b64_tr_b16 v[236:237], v199 offset:0x3e00
	v_exp_f32_e32 v75, v75
	v_exp_f32_e32 v76, v76
	v_exp_f32_e32 v77, v77
	v_exp_f32_e32 v78, v78
	s_waitcnt lgkmcnt(0)
	v_mfma_f32_32x32x16_bf16 v[16:31], v[206:209], v[222:225], v[16:31]
	v_exp_f32_e32 v79, v243
	v_pk_fma_f32 v[94:95], v[94:95], s[54:55], v[244:245] op_sel_hi:[1,0,0]
	v_mfma_f32_32x32x16_bf16 v[16:31], v[210:213], v[226:229], v[16:31]
	v_pk_fma_f32 v[92:93], v[92:93], s[54:55], v[244:245] op_sel_hi:[1,0,0]
	v_pk_fma_f32 v[90:91], v[90:91], s[54:55], v[244:245] op_sel_hi:[1,0,0]
	v_mfma_f32_32x32x16_bf16 v[16:31], v[214:217], v[230:233], v[16:31]
	v_pk_fma_f32 v[88:89], v[88:89], s[54:55], v[244:245] op_sel_hi:[1,0,0]
	v_pk_fma_f32 v[86:87], v[86:87], s[54:55], v[244:245] op_sel_hi:[1,0,0]
	v_mfma_f32_32x32x16_bf16 v[16:31], v[218:221], v[234:237], v[16:31]
	v_pk_fma_f32 v[84:85], v[84:85], s[54:55], v[244:245] op_sel_hi:[1,0,0]
	v_pk_fma_f32 v[82:83], v[82:83], s[54:55], v[244:245] op_sel_hi:[1,0,0]
	v_pk_fma_f32 v[80:81], v[80:81], s[54:55], v[244:245] op_sel_hi:[1,0,0]
	v_mov_b32_e32 v206, v242
	s_cbranch_vccz .Latt0_nrB
	s_nop 7
	s_nop 7
	s_and_saveexec_b64 s[38:39], s[4:5]
	ds_write_b32 v197, v206 offset:128
	s_or_b64 exec, exec, s[38:39]
	s_waitcnt lgkmcnt(0)
	v_add_u32_e32 v220, s77, v196
	ds_read_b128 v[208:211], v220 offset:224
	ds_read_b128 v[212:215], v220 offset:192
	ds_read_b128 v[216:219], v220 offset:160
	ds_read_b128 v[220:223], v220 offset:128
	s_waitcnt lgkmcnt(0)
	v_pk_mul_f32 v[12:13], v[12:13], v[208:209]
	v_pk_mul_f32 v[8:9], v[8:9], v[212:213]
	v_pk_mul_f32 v[4:5], v[4:5], v[216:217]
	v_pk_mul_f32 v[14:15], v[14:15], v[210:211]
	v_pk_mul_f32 v[10:11], v[10:11], v[214:215]
	v_pk_mul_f32 v[6:7], v[6:7], v[218:219]
	v_pk_mul_f32 v[2:3], v[2:3], v[222:223]
	v_pk_mul_f32 v[0:1], v[0:1], v[220:221]
	v_pk_mul_f32 v[60:61], v[60:61], v[208:209]
	v_pk_mul_f32 v[56:57], v[56:57], v[212:213]
	v_pk_mul_f32 v[52:53], v[52:53], v[216:217]
	v_pk_mul_f32 v[62:63], v[62:63], v[210:211]
	v_pk_mul_f32 v[58:59], v[58:59], v[214:215]
	v_pk_mul_f32 v[54:55], v[54:55], v[218:219]
	v_pk_mul_f32 v[50:51], v[50:51], v[222:223]
	v_pk_mul_f32 v[48:49], v[48:49], v[220:221]
	v_pk_mul_f32 v[44:45], v[44:45], v[208:209]
	v_pk_mul_f32 v[40:41], v[40:41], v[212:213]
	v_pk_mul_f32 v[36:37], v[36:37], v[216:217]
	v_pk_mul_f32 v[46:47], v[46:47], v[210:211]
	v_pk_mul_f32 v[42:43], v[42:43], v[214:215]
	v_pk_mul_f32 v[38:39], v[38:39], v[218:219]
	v_pk_mul_f32 v[34:35], v[34:35], v[222:223]
	v_pk_mul_f32 v[32:33], v[32:33], v[220:221]
	v_pk_mul_f32 v[28:29], v[28:29], v[208:209]
	v_pk_mul_f32 v[24:25], v[24:25], v[212:213]
	v_pk_mul_f32 v[20:21], v[20:21], v[216:217]
	v_pk_mul_f32 v[30:31], v[30:31], v[210:211]
	v_pk_mul_f32 v[26:27], v[26:27], v[214:215]
	v_pk_mul_f32 v[22:23], v[22:23], v[218:219]
	v_pk_mul_f32 v[18:19], v[18:19], v[222:223]
	v_pk_mul_f32 v[16:17], v[16:17], v[220:221]

.Latt0_cold_mid:
	v_lshl_add_u64 v[246:247], s[46:47], 0, v[152:153]
	s_mov_b32 m0, s95
	s_nop 0
	global_load_lds_dwordx4 v[246:247], off
	v_lshl_add_u64 v[246:247], s[46:47], 0, v[154:155]
	s_mov_b32 m0, s18
	s_nop 0
	global_load_lds_dwordx4 v[246:247], off
	v_lshl_add_u64 v[246:247], s[38:39], 0, v[156:157]
	s_mov_b32 m0, s56
	s_nop 0
	global_load_lds_dwordx4 v[246:247], off
	v_lshl_add_u64 v[246:247], s[38:39], 0, v[158:159]
	s_mov_b32 m0, s91
	s_nop 0
	global_load_lds_dwordx4 v[246:247], off
